# final combine_norm (phase 22): slot row prefetched one row ahead, expert-output loads issued ahead of the residual-row loads
# speedup vs baseline: 1.0108x; 1.0012x over previous
.LBB0_2778:
	s_cmp_lt_i32 s50, 23
	s_cselect_b64 s[0:1], -1, 0
	s_cmp_gt_i32 s51, 22
	s_cselect_b64 s[2:3], -1, 0
	s_and_b64 s[0:1], s[0:1], s[2:3]
	s_andn2_b64 vcc, exec, s[0:1]
	s_cbranch_vccnz .LBB0_2814
	v_readlane_b32 s0, v253, 63
	v_ashrrev_i32_e32 v1, 6, v0
	s_waitcnt vmcnt(0)
	v_add_u32_e32 v18, s0, v1
	s_movk_i32 s0, 0x4000
	v_cmp_gt_i32_e32 vcc, s0, v18
	s_and_saveexec_b64 s[0:1], vcc
	s_cbranch_execz .LBB0_2814
	v_and_b32_e32 v1, 63, v0
	v_lshlrev_b32_e32 v26, 4, v1
	s_waitcnt lgkmcnt(0)
	global_load_dwordx4 v[2:5], v26, s[76:77]
	global_load_dwordx4 v[6:9], v26, s[76:77] offset:1024
	global_load_dwordx4 v[10:13], v26, s[76:77] offset:2048
	global_load_dwordx4 v[14:17], v26, s[76:77] offset:3072
	v_and_b32_e32 v22, 15, v0
	v_mbcnt_lo_u32_b32 v0, -1, 0
	v_mbcnt_hi_u32_b32 v0, -1, v0
	v_and_b32_e32 v19, 64, v0
	v_add_u32_e32 v19, 64, v19
	v_xor_b32_e32 v20, 32, v0
	v_cmp_lt_i32_e32 vcc, v20, v19
	v_lshlrev_b32_e32 v24, 3, v1
	v_mov_b32_e32 v25, 0
	v_cndmask_b32_e32 v20, v0, v20, vcc
	v_lshlrev_b32_e32 v42, 2, v20
	v_xor_b32_e32 v20, 16, v0
	v_cmp_lt_i32_e32 vcc, v20, v19
	s_mov_b64 s[2:3], 0x700000
	s_ashr_i32 s71, s70, 31
	v_cndmask_b32_e32 v20, v0, v20, vcc
	v_lshlrev_b32_e32 v43, 2, v20
	v_xor_b32_e32 v20, 8, v0
	v_cmp_lt_i32_e32 vcc, v20, v19
	s_mov_b64 s[6:7], 0xc00
	s_mov_b32 s1, 0
	v_cndmask_b32_e32 v20, v0, v20, vcc
	v_lshlrev_b32_e32 v44, 2, v20
	v_xor_b32_e32 v20, 4, v0
	v_cmp_lt_i32_e32 vcc, v20, v19
	s_lshl_b64 s[4:5], s[70:71], 11
	s_mov_b64 s[8:9], 0
	v_cndmask_b32_e32 v20, v0, v20, vcc
	v_lshlrev_b32_e32 v45, 2, v20
	v_xor_b32_e32 v20, 2, v0
	v_cmp_lt_i32_e32 vcc, v20, v19
	s_mov_b32 s10, 0x800000
	s_movk_i32 s11, 0x3fff
	v_cndmask_b32_e32 v20, v0, v20, vcc
	v_lshlrev_b32_e32 v46, 2, v20
	v_xor_b32_e32 v20, 1, v0
	v_cmp_lt_i32_e32 vcc, v20, v19
	v_ashrrev_i32_e32 v19, 31, v18
	s_nop 0
	v_cndmask_b32_e32 v0, v0, v20, vcc
	v_lshlrev_b64 v[20:21], 6, v[18:19]
	v_lshl_or_b32 v20, v22, 2, v20
	v_lshlrev_b64 v[22:23], 11, v[18:19]
	v_lshlrev_b32_e32 v47, 2, v0
	v_lshl_add_u64 v[0:1], s[80:81], 0, v[24:25]
	v_or_b32_e32 v22, v22, v24
	v_lshlrev_b64 v[24:25], 12, v[18:19]
	v_or_b32_e32 v24, v24, v26
	v_lshl_add_u64 v[24:25], s[78:79], 0, v[24:25]
	v_lshl_add_u64 v[20:21], v[20:21], 0, s[2:3]
	s_lshl_b64 s[2:3], s[70:71], 6
	v_lshl_add_u64 v[24:25], v[24:25], 0, s[6:7]
	s_lshl_b64 s[6:7], s[70:71], 12
	v_mov_b32_e32 v19, 0x358637bd
	v_lshl_add_u64 v[202:203], s[48:49], 0, v[20:21]
	global_load_dword v204, v[202:203], off
	s_waitcnt vmcnt(0)
	s_branch .LBB0_2782

.LBB0_2782:
	v_lshl_add_u64 v[26:27], s[48:49], 0, v[22:23]
	v_add_co_u32_e32 v26, vcc, 0x800000, v26
	v_lshl_add_u64 v[28:29], s[48:49], 0, v[20:21]
	v_lshl_add_u64 v[202:203], v[28:29], 0, s[2:3]
	v_mov_b32_e32 v48, v204
	global_load_dword v204, v[202:203], off
	v_addc_co_u32_e32 v27, vcc, 0, v27, vcc
	v_readlane_b32 s0, v48, 0
	s_cmp_lt_i32 s0, 0
	s_cbranch_scc1 .Lcnb_0
	s_lshl_b64 s[12:13], s[0:1], 11
	v_lshl_add_u64 v[200:201], v[0:1], 0, s[12:13]
	global_load_dwordx2 v[72:73], v[200:201], off
	global_load_dwordx2 v[74:75], v[200:201], off offset:512
	global_load_dwordx2 v[76:77], v[200:201], off offset:1024
	global_load_dwordx2 v[78:79], v[200:201], off offset:1536

.Lcnb_16:
	global_load_dwordx2 v[28:29], v[26:27], off
	global_load_dwordx2 v[30:31], v[26:27], off offset:512
	global_load_dwordx2 v[32:33], v[26:27], off offset:1024
	global_load_dwordx2 v[50:51], v[26:27], off offset:1536
	s_waitcnt vmcnt(3)
	v_and_b32_e32 v38, 0xffff0000, v28
	v_readlane_b32 s0, v48, 0
	s_cmp_lt_i32 s0, 0
	v_lshlrev_b32_e32 v39, 16, v28
	v_and_b32_e32 v40, 0xffff0000, v29
	v_lshlrev_b32_e32 v41, 16, v29
	s_waitcnt vmcnt(2)
	v_and_b32_e32 v34, 0xffff0000, v30
	v_lshlrev_b32_e32 v35, 16, v30
	v_and_b32_e32 v36, 0xffff0000, v31
	v_lshlrev_b32_e32 v37, 16, v31
	s_waitcnt vmcnt(1)
	v_and_b32_e32 v30, 0xffff0000, v32
	v_lshlrev_b32_e32 v31, 16, v32
	v_and_b32_e32 v32, 0xffff0000, v33
	v_lshlrev_b32_e32 v33, 16, v33
	s_waitcnt vmcnt(0)
